# speedup vs baseline: 1.0348x; 1.0065x over previous
_Z2kA5AArgs:
	s_load_dwordx2 s[34:35], s[0:1], 0x20
	s_load_dwordx16 s[16:31], s[0:1], 0x30
	s_lshl_b32 s3, s2, 3
	v_readfirstlane_b32 s38, v0
	s_and_b32 s3, s3, 56
	s_ashr_i32 s4, s2, 5
	s_lshr_b32 s36, s38, 6
	s_add_i32 s3, s3, s4
	s_bfe_u32 s33, s2, 0x20003
	s_cmp_eq_u32 s33, 0
	s_cbranch_scc1 .Lstag_done
	s_sleep 5
